# Hyena unit set-up: shifted filter copies built by a hand-written straight-line block (batched LDS reads) instead of a 24-trip dependent loop
# speedup vs baseline: 1.0163x; 1.0163x over previous
.LBB0_928:
	v_mbcnt_lo_u32_b32 v176, -1, 0
	v_mbcnt_hi_u32_b32 v176, -1, v176
	s_getreg_b32 s6, hwreg(HW_REG_HW_ID, 0, 6)
	s_lshl_b32 s6, s6, 2
	s_and_b32 s6, s6, 0xfc
	s_or_b32 s6, s6, 0x27100
	v_mov_b32_e32 v0, s6
	s_lshl_b32 s6, s17, 5
	s_and_b32 s6, s6, 0xe0
	s_ashr_i32 s7, s17, 3
	s_or_b32 s8, s6, s7
	s_mov_b32 s6, 35
	ds_read_b32 v0, v0
	s_ashr_i32 s7, s6, 31
	s_lshl_b64 s[6:7], s[6:7], 3
	s_add_u32 s6, s0, s6
	s_addc_u32 s7, s1, s7
	s_load_dwordx2 s[10:11], s[6:7], 0x0
	s_add_i32 s6, s8, s16
	s_ashr_i32 s7, s6, 31
	s_waitcnt lgkmcnt(0)
	v_readfirstlane_b32 s9, v0
	s_lshl_b64 s[12:13], s[6:7], 14
	s_waitcnt vmcnt(0)
	v_lshl_or_b32 v0, s9, 6, v176
	s_add_u32 s9, s10, s12
	s_addc_u32 s10, s11, s13
	v_lshlrev_b32_e32 v2, 3, v0
	s_add_u32 s9, s9, 0x1003ff0
	v_ashrrev_i32_e32 v3, 31, v2
	s_addc_u32 s10, s10, 0
	v_lshlrev_b64 v[38:39], 1, v[2:3]
	v_mov_b32_e32 v3, s10
	v_sub_co_u32_e32 v4, vcc, s9, v38
	v_add_u32_e32 v2, 0x1000, v2
	s_nop 0
	v_subb_co_u32_e32 v5, vcc, v3, v39, vcc
	v_ashrrev_i32_e32 v3, 31, v2
	v_lshlrev_b64 v[2:3], 1, v[2:3]
	v_mov_b32_e32 v7, s10
	v_sub_co_u32_e32 v6, vcc, s9, v2
	s_mov_b32 s10, 35
	s_nop 0
	v_subb_co_u32_e32 v7, vcc, v7, v3, vcc
	s_barrier
	global_load_dwordx4 v[2:5], v[4:5], off
	s_nop 0
	global_load_dwordx4 v[6:9], v[6:7], off
	s_ashr_i32 s11, s10, 31
	s_lshl_b64 s[10:11], s[10:11], 3
	s_add_u32 s10, s0, s10
	s_addc_u32 s11, s1, s11
	s_load_dwordx2 s[12:13], s[10:11], 0x0
	s_ashr_i32 s9, s8, 31
	s_lshl_b64 s[10:11], s[8:9], 13
	s_mov_b32 s9, 0x34600000
	v_lshl_add_u32 v46, v0, 4, 0
	s_waitcnt lgkmcnt(0)
	s_add_u32 s12, s12, s10
	s_addc_u32 s13, s13, s11
	v_lshl_add_u64 v[10:11], s[12:13], 0, v[38:39]
	v_add_co_u32_e32 v10, vcc, s83, v10
	s_mov_b32 s12, 35
	s_nop 0
	v_addc_co_u32_e32 v11, vcc, 0, v11, vcc
	global_load_dwordx4 v[10:13], v[10:11], off
	s_ashr_i32 s13, s12, 31
	s_lshl_b64 s[12:13], s[12:13], 3
	s_add_u32 s12, s0, s12
	s_addc_u32 s13, s1, s13
	s_load_dwordx2 s[12:13], s[12:13], 0x0
	v_add_u32_e32 v47, 0x10100, v46
	s_waitcnt lgkmcnt(0)
	s_add_u32 s12, s12, s10
	s_addc_u32 s13, s13, s11
	v_lshl_add_u64 v[14:15], s[12:13], 0, v[38:39]
	v_add_co_u32_e32 v14, vcc, s9, v14
	s_mov_b32 s12, 35
	s_nop 0
	v_addc_co_u32_e32 v15, vcc, 0, v15, vcc
	global_load_dwordx4 v[14:17], v[14:15], off
	s_ashr_i32 s13, s12, 31
	s_lshl_b64 s[12:13], s[12:13], 3
	s_add_u32 s12, s0, s12
	s_addc_u32 s13, s1, s13
	s_load_dwordx2 s[12:13], s[12:13], 0x0
	s_mov_b32 s9, 0x34800000
	s_waitcnt lgkmcnt(0)
	s_add_u32 s12, s12, s10
	s_addc_u32 s13, s13, s11
	v_lshl_add_u64 v[18:19], s[12:13], 0, v[38:39]
	v_add_co_u32_e32 v18, vcc, s9, v18
	s_mov_b32 s12, 35
	s_nop 0
	v_addc_co_u32_e32 v19, vcc, 0, v19, vcc
	global_load_dwordx4 v[18:21], v[18:19], off
	s_ashr_i32 s13, s12, 31
	s_lshl_b64 s[12:13], s[12:13], 3
	s_add_u32 s12, s0, s12
	s_addc_u32 s13, s1, s13
	s_load_dwordx2 s[12:13], s[12:13], 0x0
	s_mov_b32 s9, 0x34a00000
	s_waitcnt lgkmcnt(0)
	s_add_u32 s12, s12, s10
	s_addc_u32 s13, s13, s11
	v_lshl_add_u64 v[22:23], s[12:13], 0, v[38:39]
	v_add_co_u32_e32 v22, vcc, s9, v22
	s_mov_b32 s12, 35
	s_nop 0
	v_addc_co_u32_e32 v23, vcc, 0, v23, vcc
	global_load_dwordx4 v[22:25], v[22:23], off
	s_ashr_i32 s13, s12, 31
	s_lshl_b64 s[12:13], s[12:13], 3
	s_add_u32 s12, s0, s12
	s_addc_u32 s13, s1, s13
	s_load_dwordx2 s[12:13], s[12:13], 0x0
	s_mov_b32 s9, 0x34c00000
	s_waitcnt lgkmcnt(0)
	s_add_u32 s12, s12, s10
	s_addc_u32 s13, s13, s11
	v_lshl_add_u64 v[26:27], s[12:13], 0, v[38:39]
	v_add_co_u32_e32 v26, vcc, s9, v26
	s_mov_b32 s12, 35
	s_nop 0
	v_addc_co_u32_e32 v27, vcc, 0, v27, vcc
	global_load_dwordx4 v[26:29], v[26:27], off
	s_ashr_i32 s13, s12, 31
	s_lshl_b64 s[12:13], s[12:13], 3
	s_add_u32 s12, s0, s12
	s_addc_u32 s13, s1, s13
	s_load_dwordx2 s[12:13], s[12:13], 0x0
	s_mov_b32 s9, 0x34e00000
	s_waitcnt lgkmcnt(0)
	s_add_u32 s12, s12, s10
	s_addc_u32 s13, s13, s11
	v_lshl_add_u64 v[30:31], s[12:13], 0, v[38:39]
	v_add_co_u32_e32 v30, vcc, s9, v30
	s_mov_b32 s12, 35
	s_nop 0
	v_addc_co_u32_e32 v31, vcc, 0, v31, vcc
	global_load_dwordx4 v[30:33], v[30:31], off
	s_ashr_i32 s13, s12, 31
	s_lshl_b64 s[12:13], s[12:13], 3
	s_add_u32 s12, s0, s12
	s_addc_u32 s13, s1, s13
	s_load_dwordx2 s[12:13], s[12:13], 0x0
	s_mov_b32 s9, 0x35000000
	s_waitcnt lgkmcnt(0)
	s_add_u32 s12, s12, s10
	s_addc_u32 s13, s13, s11
	v_lshl_add_u64 v[34:35], s[12:13], 0, v[38:39]
	v_add_co_u32_e32 v34, vcc, s9, v34
	s_mov_b32 s12, 35
	s_nop 0
	v_addc_co_u32_e32 v35, vcc, 0, v35, vcc
	global_load_dwordx4 v[34:37], v[34:35], off
	s_ashr_i32 s13, s12, 31
	s_lshl_b64 s[12:13], s[12:13], 3
	s_add_u32 s12, s0, s12
	s_addc_u32 s13, s1, s13
	s_load_dwordx2 s[12:13], s[12:13], 0x0
	s_mov_b32 s9, 0x35200000
	s_waitcnt lgkmcnt(0)
	s_add_u32 s10, s12, s10
	s_addc_u32 s11, s13, s11
	v_lshl_add_u64 v[38:39], s[10:11], 0, v[38:39]
	v_add_co_u32_e32 v38, vcc, s9, v38
	v_readfirstlane_b32 s9, v0
	s_nop 0
	v_addc_co_u32_e32 v39, vcc, 0, v39, vcc
	global_load_dwordx4 v[38:41], v[38:39], off
	v_cmp_gt_i32_e32 vcc, 32, v0
	s_waitcnt vmcnt(9)
	v_alignbit_b32 v42, v5, v5, 16
	v_alignbit_b32 v43, v4, v4, 16
	v_alignbit_b32 v44, v3, v3, 16
	v_alignbit_b32 v45, v2, v2, 16
	s_waitcnt vmcnt(8)
	v_alignbit_b32 v2, v9, v9, 16
	v_alignbit_b32 v3, v8, v8, 16
	v_alignbit_b32 v4, v7, v7, 16
	v_alignbit_b32 v5, v6, v6, 16
	ds_write_b128 v46, v[42:45]
	ds_write_b128 v46, v[2:5] offset:8192
	s_waitcnt vmcnt(7)
	ds_write_b128 v47, v[10:13]
	s_waitcnt vmcnt(6)
	ds_write_b128 v47, v[14:17] offset:8224
	s_waitcnt vmcnt(5)
	ds_write_b128 v47, v[18:21] offset:16448
	s_waitcnt vmcnt(4)
	ds_write_b128 v47, v[22:25] offset:24672
	s_waitcnt vmcnt(3)
	ds_write_b128 v47, v[26:29] offset:32896
	s_waitcnt vmcnt(2)
	ds_write_b128 v47, v[30:33] offset:41120
	s_waitcnt vmcnt(1)
	ds_write_b128 v47, v[34:37] offset:49344
	s_waitcnt vmcnt(0)
	ds_write_b128 v47, v[38:41] offset:57568
	s_and_saveexec_b64 s[10:11], vcc
	v_lshl_add_u32 v2, v0, 2, 0
	v_add_u32_e32 v2, 0x20200, v2
	ds_write_b32 v2, v1
	s_or_b64 exec, exec, s[10:11]
	s_movk_i32 s10, 0x3000
	v_cmp_gt_i32_e32 vcc, s10, v0
	s_waitcnt lgkmcnt(0)
	s_barrier
	v_lshlrev_b32_e32 v2, 2, v0
	v_cmp_gt_u32_e32 vcc, 511, v0
	s_movk_i32 s14, 0x1fe
	v_cmp_gt_u32_e64 s[12:13], s14, v0
	ds_read_b32 v3, v2
	ds_read_b32 v4, v2 offset:4
	ds_read_b32 v5, v2 offset:8
	ds_read_b32 v6, v2 offset:2048
	ds_read_b32 v7, v2 offset:2052
	ds_read_b32 v8, v2 offset:2056
	ds_read_b32 v9, v2 offset:4096
	ds_read_b32 v10, v2 offset:4100
	ds_read_b32 v11, v2 offset:4104
	ds_read_b32 v12, v2 offset:6144
	ds_read_b32 v13, v2 offset:6148
	ds_read_b32 v14, v2 offset:6152
	s_waitcnt lgkmcnt(0)
	v_alignbit_b32 v15, v4, v3, 16
	v_alignbit_b32 v16, v5, v4, 16
	v_alignbit_b32 v17, v7, v6, 16
	v_alignbit_b32 v18, v8, v7, 16
	v_alignbit_b32 v19, v10, v9, 16
	v_alignbit_b32 v20, v11, v10, 16
	v_alignbit_b32 v21, v13, v12, 16
	v_alignbit_b32 v22, v14, v13, 16
	ds_write_b32 v2, v15 offset:16448
	ds_write_b32 v2, v4 offset:32896
	ds_write_b32 v2, v16 offset:49344
	ds_write_b32 v2, v17 offset:18496
	ds_write_b32 v2, v7 offset:34944
	ds_write_b32 v2, v18 offset:51392
	ds_write_b32 v2, v19 offset:20544
	ds_write_b32 v2, v10 offset:36992
	ds_write_b32 v2, v20 offset:53440
	ds_write_b32 v2, v21 offset:22592
	ds_write_b32 v2, v13 offset:39040
	ds_write_b32 v2, v22 offset:55488
	ds_read_b32 v3, v2 offset:8192
	ds_read_b32 v4, v2 offset:8196
	ds_read_b32 v5, v2 offset:8200
	ds_read_b32 v6, v2 offset:10240
	ds_read_b32 v7, v2 offset:10244
	ds_read_b32 v8, v2 offset:10248
	ds_read_b32 v9, v2 offset:12288
	ds_read_b32 v10, v2 offset:12292
	ds_read_b32 v11, v2 offset:12296
	ds_read_b32 v12, v2 offset:14336
	ds_read_b32 v13, v2 offset:14340
	ds_read_b32 v14, v2 offset:14344
	s_waitcnt lgkmcnt(0)
	v_cndmask_b32_e32 v13, v1, v13, vcc
	v_cndmask_b32_e64 v14, v1, v14, s[12:13]
	v_alignbit_b32 v15, v4, v3, 16
	v_alignbit_b32 v16, v5, v4, 16
	v_alignbit_b32 v17, v7, v6, 16
	v_alignbit_b32 v18, v8, v7, 16
	v_alignbit_b32 v19, v10, v9, 16
	v_alignbit_b32 v20, v11, v10, 16
	v_alignbit_b32 v21, v13, v12, 16
	v_alignbit_b32 v22, v14, v13, 16
	ds_write_b32 v2, v15 offset:24640
	ds_write_b32 v2, v4 offset:41088
	ds_write_b32 v2, v16 offset:57536
	ds_write_b32 v2, v17 offset:26688
	ds_write_b32 v2, v7 offset:43136
	ds_write_b32 v2, v18 offset:59584
	ds_write_b32 v2, v19 offset:28736
	ds_write_b32 v2, v10 offset:45184
	ds_write_b32 v2, v20 offset:61632
	ds_write_b32 v2, v21 offset:30784
	ds_write_b32 v2, v13 offset:47232
	ds_write_b32 v2, v22 offset:63680
.LBB0_935:
	s_mov_b32 s10, 35
	s_waitcnt lgkmcnt(0)
	s_barrier
	s_ashr_i32 s11, s10, 31
	s_ashr_i32 s12, s9, 6
	s_lshl_b64 s[10:11], s[10:11], 3
	s_add_u32 s10, s0, s10
	s_addc_u32 s11, s1, s11
	s_load_dwordx2 s[10:11], s[10:11], 0x0
	v_bfe_u32 v9, v176, 1, 3
	v_lshl_add_u32 v2, v9, 8, s8
	v_and_b32_e32 v177, 1, v176
	v_ashrrev_i32_e32 v3, 31, v2
	v_bfe_u32 v8, v0, 4, 2
	v_lshlrev_b64 v[4:5], 13, v[2:3]
	v_lshlrev_b32_e32 v6, 6, v177
	v_lshlrev_b32_e32 v172, 3, v8
	s_waitcnt lgkmcnt(0)
	v_lshl_add_u64 v[4:5], s[10:11], 0, v[4:5]
	v_mov_b32_e32 v173, v1
	v_lshl_or_b32 v6, s12, 9, v6
	v_lshl_add_u64 v[4:5], v[4:5], 0, v[172:173]
	v_ashrrev_i32_e32 v7, 31, v6
	v_lshl_add_u64 v[4:5], v[6:7], 1, v[4:5]
	s_mov_b64 s[8:9], 0x35400000
	v_lshl_add_u64 v[6:7], v[4:5], 0, s[8:9]
	s_mov_b32 s8, 0x35400000
	v_add_co_u32_e32 v4, vcc, s8, v4
	s_movk_i32 s8, 0xffc
	s_nop 0
	v_addc_co_u32_e32 v5, vcc, 0, v5, vcc
	global_load_dwordx2 v[168:169], v[6:7], off offset:32
	global_load_dwordx2 v[166:167], v[6:7], off offset:64
	global_load_dwordx2 v[164:165], v[6:7], off offset:96
	global_load_dwordx2 v[162:163], v[6:7], off offset:256
	global_load_dwordx2 v[160:161], v[6:7], off offset:288
	global_load_dwordx2 v[158:159], v[6:7], off offset:320
	global_load_dwordx2 v[156:157], v[6:7], off offset:352
	global_load_dwordx2 v[154:155], v[6:7], off offset:512
	global_load_dwordx2 v[152:153], v[6:7], off offset:544
	global_load_dwordx2 v[150:151], v[6:7], off offset:576
	global_load_dwordx2 v[148:149], v[6:7], off offset:608
	global_load_dwordx2 v[146:147], v[6:7], off offset:768
	global_load_dwordx2 v[170:171], v[4:5], off
	global_load_dwordx2 v[144:145], v[6:7], off offset:800
	global_load_dwordx2 v[142:143], v[6:7], off offset:832
	global_load_dwordx2 v[140:141], v[6:7], off offset:864
	v_and_b32_e32 v4, 15, v176
	v_mov_b32_e32 v5, 0xfff
	v_lshrrev_b32_e32 v173, 4, v0
	v_bitop3_b32 v0, v4, 3, v5 bitop3:0x48
	v_bitop3_b32 v4, v4, s8, v5 bitop3:0x48
	v_add_u32_e32 v4, v172, v4
	v_mul_u32_u24_e32 v178, 0x2020, v9
	v_lshlrev_b32_e32 v179, 4, v8
	v_lshlrev_b64 v[174:175], 12, v[2:3]
	v_mul_u32_u24_e32 v0, 0x4040, v0
	s_lshl_b32 s18, s12, 3
	s_sub_i32 s20, s18, 63
	v_lshl_add_u32 v180, v4, 1, v0
	s_lshl_b32 s8, s20, 7
	v_subrev_u32_e32 v0, s8, v180
	v_add_u32_e32 v0, 0, v0
	v_subrev_u32_e32 v2, 32, v0
	ds_read_b64 v[124:125], v0 offset:64
	ds_read_b64 v[126:127], v0 offset:72
	ds_read_b64 v[128:129], v0 offset:32
	ds_read_b64 v[130:131], v0 offset:40
	ds_read_b64 v[132:133], v0
	ds_read_b64 v[134:135], v0 offset:8
	ds_read_b64 v[136:137], v2
	v_subrev_u32_e32 v2, 24, v0
	ds_read_b64 v[138:139], v2
	v_subrev_u32_e32 v2, 64, v0
	ds_read_b64 v[68:69], v2
	v_subrev_u32_e32 v2, 56, v0
	ds_read_b64 v[70:71], v2
	v_add_u32_e32 v2, 0xffffffa0, v0
	v_add_u32_e32 v0, 0xffffffa8, v0
	ds_read_b64 v[72:73], v2
	ds_read_b64 v[74:75], v0
	v_lshlrev_b32_e32 v0, 7, v177
	s_movk_i32 s8, 0x2020
	v_mad_u32_u24 v0, v9, s8, v0
	s_mov_b32 s8, 0x12080
	v_mov_b32_e32 v2, v1
	v_mov_b32_e32 v3, v1
	v_add3_u32 v184, v0, v179, s8
	v_mov_b32_e32 v0, v1
	v_mov_b64_e32 v[6:7], v[2:3]
	v_mov_b64_e32 v[22:23], v[2:3]
	v_mov_b64_e32 v[38:39], v[2:3]
	v_mov_b64_e32 v[54:55], v[2:3]
	v_mov_b64_e32 v[10:11], v[2:3]
	v_mov_b64_e32 v[26:27], v[2:3]
	v_mov_b64_e32 v[42:43], v[2:3]
	v_mov_b64_e32 v[58:59], v[2:3]
	v_mov_b64_e32 v[14:15], v[2:3]
	v_mov_b64_e32 v[30:31], v[2:3]
	v_mov_b64_e32 v[46:47], v[2:3]
	v_mov_b64_e32 v[62:63], v[2:3]
	v_mov_b64_e32 v[18:19], v[2:3]
	v_mov_b64_e32 v[34:35], v[2:3]
	v_mov_b64_e32 v[50:51], v[2:3]
	v_mov_b64_e32 v[66:67], v[2:3]
	s_or_b32 s19, s18, 7
	v_subrev_u32_e32 v183, 32, v180
	v_subrev_u32_e32 v182, 64, v180
	v_add_u32_e32 v181, 0xffffffa0, v180
	s_movk_i32 s21, 0x46
	v_mov_b64_e32 v[4:5], v[0:1]
	v_mov_b64_e32 v[20:21], v[0:1]
	v_mov_b64_e32 v[36:37], v[0:1]
	v_mov_b64_e32 v[52:53], v[0:1]
	v_mov_b64_e32 v[8:9], v[0:1]
	v_mov_b64_e32 v[24:25], v[0:1]
	v_mov_b64_e32 v[40:41], v[0:1]
	v_mov_b64_e32 v[56:57], v[0:1]
	v_mov_b64_e32 v[12:13], v[0:1]
	v_mov_b64_e32 v[28:29], v[0:1]
	v_mov_b64_e32 v[44:45], v[0:1]
	v_mov_b64_e32 v[60:61], v[0:1]
	v_mov_b64_e32 v[16:17], v[0:1]
	v_mov_b64_e32 v[32:33], v[0:1]
	v_mov_b64_e32 v[48:49], v[0:1]
	v_mov_b64_e32 v[64:65], v[0:1]
